# P8 gate_up epilogue: SwiGLU constants folded into the bias fma (9 instead of 11.5 VALU slots per output), f32 throughout
# speedup vs baseline: 1.0049x; 1.0008x over previous
.LBB0_1352:
	s_nop 15
	s_nop 15
	v_lshl_add_u32 v2, s55, 10, v194
	ds_read_b128 v[14:17], v2
	ds_read_b128 v[6:9], v2 offset:16
	ds_read_b128 v[10:13], v2 offset:512
	ds_read_b128 v[2:5], v2 offset:528
	v_mov_b32_e32 v18, 0xbd1d265f
	v_mov_b32_e32 v20, 0xbbd083aa
	v_mov_b32_e32 v32, 0xc01d265f
	v_mov_b32_e32 v30, 0xbed083aa
	v_mov_b32_e32 v33, 0xc05083aa
	v_mov_b32_e32 v19, 0x401c62c0
	v_lshl_add_u32 v24, s53, 8, v177
	v_lshl_or_b32 v22, s54, 7, v195
	v_lshl_add_u32 v21, v24, 11, v22
	s_waitcnt lgkmcnt(0)
	v_pk_mul_f32 v[14:15], v[14:15], v[32:33] op_sel_hi:[1,0]
	v_pk_mul_f32 v[16:17], v[16:17], v[32:33] op_sel_hi:[1,0]
	v_pk_mul_f32 v[6:7], v[6:7], v[32:33] op_sel_hi:[1,0]
	v_pk_mul_f32 v[8:9], v[8:9], v[32:33] op_sel_hi:[1,0]
	v_pk_fma_f32 v[10:11], v[10:11], v[30:31], v[30:31] op_sel_hi:[1,0,0]
	v_pk_fma_f32 v[12:13], v[12:13], v[30:31], v[30:31] op_sel_hi:[1,0,0]
	v_pk_fma_f32 v[2:3], v[2:3], v[30:31], v[30:31] op_sel_hi:[1,0,0]
	v_pk_fma_f32 v[4:5], v[4:5], v[30:31], v[30:31] op_sel_hi:[1,0,0]
	v_pk_fma_f32 v[158:159], v[158:159], v[18:19], v[14:15] op_sel_hi:[1,0,1]
	v_pk_fma_f32 v[160:161], v[160:161], v[18:19], v[16:17] op_sel_hi:[1,0,1]
	v_pk_fma_f32 v[150:151], v[150:151], v[18:19], v[6:7] op_sel_hi:[1,0,1]
	v_pk_fma_f32 v[152:153], v[152:153], v[18:19], v[8:9] op_sel_hi:[1,0,1]
	v_max_f32_e32 v158, 0xc1898193, v158
	v_max_f32_e32 v159, 0xc1898193, v159
	v_max_f32_e32 v160, 0xc1898193, v160
	v_max_f32_e32 v161, 0xc1898193, v161
	v_max_f32_e32 v150, 0xc1898193, v150
	v_max_f32_e32 v151, 0xc1898193, v151
	v_max_f32_e32 v152, 0xc1898193, v152
	v_max_f32_e32 v153, 0xc1898193, v153
	v_exp_f32_e32 v22, v158
	v_exp_f32_e32 v23, v159
	v_exp_f32_e32 v24, v160
	v_exp_f32_e32 v25, v161
	v_exp_f32_e32 v26, v150
	v_exp_f32_e32 v27, v151
	v_exp_f32_e32 v28, v152
	v_exp_f32_e32 v29, v153
	v_pk_fma_f32 v[154:155], v[154:155], v[20:21], v[10:11] op_sel_hi:[1,0,1]
	v_pk_fma_f32 v[156:157], v[156:157], v[20:21], v[12:13] op_sel_hi:[1,0,1]
	v_pk_fma_f32 v[146:147], v[146:147], v[20:21], v[2:3] op_sel_hi:[1,0,1]
	v_pk_fma_f32 v[148:149], v[148:149], v[20:21], v[4:5] op_sel_hi:[1,0,1]
	v_pk_add_f32 v[22:23], v[22:23], 1.0 op_sel_hi:[1,0]
	v_pk_add_f32 v[24:25], v[24:25], 1.0 op_sel_hi:[1,0]
	v_pk_add_f32 v[26:27], v[26:27], 1.0 op_sel_hi:[1,0]
	v_pk_add_f32 v[28:29], v[28:29], 1.0 op_sel_hi:[1,0]
	v_rcp_f32_e32 v22, v22
	v_rcp_f32_e32 v23, v23
	v_rcp_f32_e32 v24, v24
	v_rcp_f32_e32 v25, v25
	v_rcp_f32_e32 v26, v26
	v_rcp_f32_e32 v27, v27
	v_rcp_f32_e32 v28, v28
	v_rcp_f32_e32 v29, v29
	v_med3_f32 v154, v154, v33, v19
	v_med3_f32 v155, v155, v33, v19
	v_med3_f32 v156, v156, v33, v19
	v_med3_f32 v157, v157, v33, v19
	v_med3_f32 v146, v146, v33, v19
	v_med3_f32 v147, v147, v33, v19
	v_med3_f32 v148, v148, v33, v19
	v_med3_f32 v149, v149, v33, v19
	v_pk_mul_f32 v[158:159], v[158:159], v[22:23]
	v_pk_mul_f32 v[160:161], v[160:161], v[24:25]
	v_pk_mul_f32 v[150:151], v[150:151], v[26:27]
	v_pk_mul_f32 v[152:153], v[152:153], v[28:29]
	v_pk_mul_f32 v[158:159], v[158:159], v[154:155]
	v_pk_mul_f32 v[160:161], v[160:161], v[156:157]
	v_pk_mul_f32 v[150:151], v[150:151], v[146:147]
	v_pk_mul_f32 v[152:153], v[152:153], v[148:149]
	v_cvt_pk_fp8_f32 v22, v158, v159
	v_cvt_pk_fp8_f32 v23, v150, v151
	v_cvt_pk_fp8_f32 v22, v160, v161 op_sel:[0,0,1]
	v_cvt_pk_fp8_f32 v23, v152, v153 op_sel:[0,0,1]
	s_nop 1
	global_store_dwordx2 v21, v[22:23], s[0:1]
	v_pk_fma_f32 v[142:143], v[142:143], v[18:19], v[14:15] op_sel_hi:[1,0,1]
	v_pk_fma_f32 v[144:145], v[144:145], v[18:19], v[16:17] op_sel_hi:[1,0,1]
	v_pk_fma_f32 v[134:135], v[134:135], v[18:19], v[6:7] op_sel_hi:[1,0,1]
	v_pk_fma_f32 v[136:137], v[136:137], v[18:19], v[8:9] op_sel_hi:[1,0,1]
	v_max_f32_e32 v142, 0xc1898193, v142
	v_max_f32_e32 v143, 0xc1898193, v143
	v_max_f32_e32 v144, 0xc1898193, v144
	v_max_f32_e32 v145, 0xc1898193, v145
	v_max_f32_e32 v134, 0xc1898193, v134
	v_max_f32_e32 v135, 0xc1898193, v135
	v_max_f32_e32 v136, 0xc1898193, v136
	v_max_f32_e32 v137, 0xc1898193, v137
	v_exp_f32_e32 v22, v142
	v_exp_f32_e32 v23, v143
	v_exp_f32_e32 v24, v144
	v_exp_f32_e32 v25, v145
	v_exp_f32_e32 v26, v134
	v_exp_f32_e32 v27, v135
	v_exp_f32_e32 v28, v136
	v_exp_f32_e32 v29, v137
	v_pk_fma_f32 v[138:139], v[138:139], v[20:21], v[10:11] op_sel_hi:[1,0,1]
	v_pk_fma_f32 v[140:141], v[140:141], v[20:21], v[12:13] op_sel_hi:[1,0,1]
	v_pk_fma_f32 v[130:131], v[130:131], v[20:21], v[2:3] op_sel_hi:[1,0,1]
	v_pk_fma_f32 v[132:133], v[132:133], v[20:21], v[4:5] op_sel_hi:[1,0,1]
	v_pk_add_f32 v[22:23], v[22:23], 1.0 op_sel_hi:[1,0]
	v_pk_add_f32 v[24:25], v[24:25], 1.0 op_sel_hi:[1,0]
	v_pk_add_f32 v[26:27], v[26:27], 1.0 op_sel_hi:[1,0]
	v_pk_add_f32 v[28:29], v[28:29], 1.0 op_sel_hi:[1,0]
	v_rcp_f32_e32 v22, v22
	v_rcp_f32_e32 v23, v23
	v_rcp_f32_e32 v24, v24
	v_rcp_f32_e32 v25, v25
	v_rcp_f32_e32 v26, v26
	v_rcp_f32_e32 v27, v27
	v_rcp_f32_e32 v28, v28
	v_rcp_f32_e32 v29, v29
	v_med3_f32 v138, v138, v33, v19
	v_med3_f32 v139, v139, v33, v19
	v_med3_f32 v140, v140, v33, v19
	v_med3_f32 v141, v141, v33, v19
	v_med3_f32 v130, v130, v33, v19
	v_med3_f32 v131, v131, v33, v19
	v_med3_f32 v132, v132, v33, v19
	v_med3_f32 v133, v133, v33, v19
	v_pk_mul_f32 v[142:143], v[142:143], v[22:23]
	v_pk_mul_f32 v[144:145], v[144:145], v[24:25]
	v_pk_mul_f32 v[134:135], v[134:135], v[26:27]
	v_pk_mul_f32 v[136:137], v[136:137], v[28:29]
	v_pk_mul_f32 v[142:143], v[142:143], v[138:139]
	v_pk_mul_f32 v[144:145], v[144:145], v[140:141]
	v_pk_mul_f32 v[134:135], v[134:135], v[130:131]
	v_pk_mul_f32 v[136:137], v[136:137], v[132:133]
	v_cvt_pk_fp8_f32 v26, v142, v143
	v_cvt_pk_fp8_f32 v27, v134, v135
	v_cvt_pk_fp8_f32 v26, v144, v145 op_sel:[0,0,1]
	v_cvt_pk_fp8_f32 v27, v136, v137 op_sel:[0,0,1]
	v_add_u32_e32 v31, 0x8000, v21
	s_nop 0
	global_store_dwordx2 v31, v[26:27], s[0:1]
	v_pk_fma_f32 v[126:127], v[126:127], v[18:19], v[14:15] op_sel_hi:[1,0,1]
	v_pk_fma_f32 v[128:129], v[128:129], v[18:19], v[16:17] op_sel_hi:[1,0,1]
	v_pk_fma_f32 v[118:119], v[118:119], v[18:19], v[6:7] op_sel_hi:[1,0,1]
	v_pk_fma_f32 v[120:121], v[120:121], v[18:19], v[8:9] op_sel_hi:[1,0,1]
	v_max_f32_e32 v126, 0xc1898193, v126
	v_max_f32_e32 v127, 0xc1898193, v127
	v_max_f32_e32 v128, 0xc1898193, v128
	v_max_f32_e32 v129, 0xc1898193, v129
	v_max_f32_e32 v118, 0xc1898193, v118
	v_max_f32_e32 v119, 0xc1898193, v119
	v_max_f32_e32 v120, 0xc1898193, v120
	v_max_f32_e32 v121, 0xc1898193, v121
	v_exp_f32_e32 v22, v126
	v_exp_f32_e32 v23, v127
	v_exp_f32_e32 v24, v128
	v_exp_f32_e32 v25, v129
	v_exp_f32_e32 v26, v118
	v_exp_f32_e32 v27, v119
	v_exp_f32_e32 v28, v120
	v_exp_f32_e32 v29, v121
	v_pk_fma_f32 v[122:123], v[122:123], v[20:21], v[10:11] op_sel_hi:[1,0,1]
	v_pk_fma_f32 v[124:125], v[124:125], v[20:21], v[12:13] op_sel_hi:[1,0,1]
	v_pk_fma_f32 v[114:115], v[114:115], v[20:21], v[2:3] op_sel_hi:[1,0,1]
	v_pk_fma_f32 v[116:117], v[116:117], v[20:21], v[4:5] op_sel_hi:[1,0,1]
	v_pk_add_f32 v[22:23], v[22:23], 1.0 op_sel_hi:[1,0]
	v_pk_add_f32 v[24:25], v[24:25], 1.0 op_sel_hi:[1,0]
	v_pk_add_f32 v[26:27], v[26:27], 1.0 op_sel_hi:[1,0]
	v_pk_add_f32 v[28:29], v[28:29], 1.0 op_sel_hi:[1,0]
	v_rcp_f32_e32 v22, v22
	v_rcp_f32_e32 v23, v23
	v_rcp_f32_e32 v24, v24
	v_rcp_f32_e32 v25, v25
	v_rcp_f32_e32 v26, v26
	v_rcp_f32_e32 v27, v27
	v_rcp_f32_e32 v28, v28
	v_rcp_f32_e32 v29, v29
	v_med3_f32 v122, v122, v33, v19
	v_med3_f32 v123, v123, v33, v19
	v_med3_f32 v124, v124, v33, v19
	v_med3_f32 v125, v125, v33, v19
	v_med3_f32 v114, v114, v33, v19
	v_med3_f32 v115, v115, v33, v19
	v_med3_f32 v116, v116, v33, v19
	v_med3_f32 v117, v117, v33, v19
	v_pk_mul_f32 v[126:127], v[126:127], v[22:23]
	v_pk_mul_f32 v[128:129], v[128:129], v[24:25]
	v_pk_mul_f32 v[118:119], v[118:119], v[26:27]
	v_pk_mul_f32 v[120:121], v[120:121], v[28:29]
	v_pk_mul_f32 v[126:127], v[126:127], v[122:123]
	v_pk_mul_f32 v[128:129], v[128:129], v[124:125]
	v_pk_mul_f32 v[118:119], v[118:119], v[114:115]
	v_pk_mul_f32 v[120:121], v[120:121], v[116:117]
	v_cvt_pk_fp8_f32 v22, v126, v127
	v_cvt_pk_fp8_f32 v23, v118, v119
	v_cvt_pk_fp8_f32 v22, v128, v129 op_sel:[0,0,1]
	v_cvt_pk_fp8_f32 v23, v120, v121 op_sel:[0,0,1]
	v_add_u32_e32 v31, 0x10000, v21
	s_nop 0
	global_store_dwordx2 v31, v[22:23], s[0:1]
	v_pk_fma_f32 v[110:111], v[110:111], v[18:19], v[14:15] op_sel_hi:[1,0,1]
	v_pk_fma_f32 v[112:113], v[112:113], v[18:19], v[16:17] op_sel_hi:[1,0,1]
	v_pk_fma_f32 v[102:103], v[102:103], v[18:19], v[6:7] op_sel_hi:[1,0,1]
	v_pk_fma_f32 v[104:105], v[104:105], v[18:19], v[8:9] op_sel_hi:[1,0,1]
	v_max_f32_e32 v110, 0xc1898193, v110
	v_max_f32_e32 v111, 0xc1898193, v111
	v_max_f32_e32 v112, 0xc1898193, v112
	v_max_f32_e32 v113, 0xc1898193, v113
	v_max_f32_e32 v102, 0xc1898193, v102
	v_max_f32_e32 v103, 0xc1898193, v103
	v_max_f32_e32 v104, 0xc1898193, v104
	v_max_f32_e32 v105, 0xc1898193, v105
	v_exp_f32_e32 v22, v110
	v_exp_f32_e32 v23, v111
	v_exp_f32_e32 v24, v112
	v_exp_f32_e32 v25, v113
	v_exp_f32_e32 v26, v102
	v_exp_f32_e32 v27, v103
	v_exp_f32_e32 v28, v104
	v_exp_f32_e32 v29, v105
	v_pk_fma_f32 v[106:107], v[106:107], v[20:21], v[10:11] op_sel_hi:[1,0,1]
	v_pk_fma_f32 v[108:109], v[108:109], v[20:21], v[12:13] op_sel_hi:[1,0,1]
	v_pk_fma_f32 v[98:99], v[98:99], v[20:21], v[2:3] op_sel_hi:[1,0,1]
	v_pk_fma_f32 v[100:101], v[100:101], v[20:21], v[4:5] op_sel_hi:[1,0,1]
	v_pk_add_f32 v[22:23], v[22:23], 1.0 op_sel_hi:[1,0]
	v_pk_add_f32 v[24:25], v[24:25], 1.0 op_sel_hi:[1,0]
	v_pk_add_f32 v[26:27], v[26:27], 1.0 op_sel_hi:[1,0]
	v_pk_add_f32 v[28:29], v[28:29], 1.0 op_sel_hi:[1,0]
	v_rcp_f32_e32 v22, v22
	v_rcp_f32_e32 v23, v23
	v_rcp_f32_e32 v24, v24
	v_rcp_f32_e32 v25, v25
	v_rcp_f32_e32 v26, v26
	v_rcp_f32_e32 v27, v27
	v_rcp_f32_e32 v28, v28
	v_rcp_f32_e32 v29, v29
	v_med3_f32 v106, v106, v33, v19
	v_med3_f32 v107, v107, v33, v19
	v_med3_f32 v108, v108, v33, v19
	v_med3_f32 v109, v109, v33, v19
	v_med3_f32 v98, v98, v33, v19
	v_med3_f32 v99, v99, v33, v19
	v_med3_f32 v100, v100, v33, v19
	v_med3_f32 v101, v101, v33, v19
	v_pk_mul_f32 v[110:111], v[110:111], v[22:23]
	v_pk_mul_f32 v[112:113], v[112:113], v[24:25]
	v_pk_mul_f32 v[102:103], v[102:103], v[26:27]
	v_pk_mul_f32 v[104:105], v[104:105], v[28:29]
	v_pk_mul_f32 v[110:111], v[110:111], v[106:107]
	v_pk_mul_f32 v[112:113], v[112:113], v[108:109]
	v_pk_mul_f32 v[102:103], v[102:103], v[98:99]
	v_pk_mul_f32 v[104:105], v[104:105], v[100:101]
	v_cvt_pk_fp8_f32 v26, v110, v111
	v_cvt_pk_fp8_f32 v27, v102, v103
	v_cvt_pk_fp8_f32 v26, v112, v113 op_sel:[0,0,1]
	v_cvt_pk_fp8_f32 v27, v104, v105 op_sel:[0,0,1]
	v_add_u32_e32 v31, 0x18000, v21
	s_nop 0
	global_store_dwordx2 v31, v[26:27], s[0:1]
	v_pk_fma_f32 v[94:95], v[94:95], v[18:19], v[14:15] op_sel_hi:[1,0,1]
	v_pk_fma_f32 v[96:97], v[96:97], v[18:19], v[16:17] op_sel_hi:[1,0,1]
	v_pk_fma_f32 v[86:87], v[86:87], v[18:19], v[6:7] op_sel_hi:[1,0,1]
	v_pk_fma_f32 v[88:89], v[88:89], v[18:19], v[8:9] op_sel_hi:[1,0,1]
	v_max_f32_e32 v94, 0xc1898193, v94
	v_max_f32_e32 v95, 0xc1898193, v95
	v_max_f32_e32 v96, 0xc1898193, v96
	v_max_f32_e32 v97, 0xc1898193, v97
	v_max_f32_e32 v86, 0xc1898193, v86
	v_max_f32_e32 v87, 0xc1898193, v87
	v_max_f32_e32 v88, 0xc1898193, v88
	v_max_f32_e32 v89, 0xc1898193, v89
	v_exp_f32_e32 v22, v94
	v_exp_f32_e32 v23, v95
	v_exp_f32_e32 v24, v96
	v_exp_f32_e32 v25, v97
	v_exp_f32_e32 v26, v86
	v_exp_f32_e32 v27, v87
	v_exp_f32_e32 v28, v88
	v_exp_f32_e32 v29, v89
	v_pk_fma_f32 v[90:91], v[90:91], v[20:21], v[10:11] op_sel_hi:[1,0,1]
	v_pk_fma_f32 v[92:93], v[92:93], v[20:21], v[12:13] op_sel_hi:[1,0,1]
	v_pk_fma_f32 v[82:83], v[82:83], v[20:21], v[2:3] op_sel_hi:[1,0,1]
	v_pk_fma_f32 v[84:85], v[84:85], v[20:21], v[4:5] op_sel_hi:[1,0,1]
	v_pk_add_f32 v[22:23], v[22:23], 1.0 op_sel_hi:[1,0]
	v_pk_add_f32 v[24:25], v[24:25], 1.0 op_sel_hi:[1,0]
	v_pk_add_f32 v[26:27], v[26:27], 1.0 op_sel_hi:[1,0]
	v_pk_add_f32 v[28:29], v[28:29], 1.0 op_sel_hi:[1,0]
	v_rcp_f32_e32 v22, v22
	v_rcp_f32_e32 v23, v23
	v_rcp_f32_e32 v24, v24
	v_rcp_f32_e32 v25, v25
	v_rcp_f32_e32 v26, v26
	v_rcp_f32_e32 v27, v27
	v_rcp_f32_e32 v28, v28
	v_rcp_f32_e32 v29, v29
	v_med3_f32 v90, v90, v33, v19
	v_med3_f32 v91, v91, v33, v19
	v_med3_f32 v92, v92, v33, v19
	v_med3_f32 v93, v93, v33, v19
	v_med3_f32 v82, v82, v33, v19
	v_med3_f32 v83, v83, v33, v19
	v_med3_f32 v84, v84, v33, v19
	v_med3_f32 v85, v85, v33, v19
	v_pk_mul_f32 v[94:95], v[94:95], v[22:23]
	v_pk_mul_f32 v[96:97], v[96:97], v[24:25]
	v_pk_mul_f32 v[86:87], v[86:87], v[26:27]
	v_pk_mul_f32 v[88:89], v[88:89], v[28:29]
	v_pk_mul_f32 v[94:95], v[94:95], v[90:91]
	v_pk_mul_f32 v[96:97], v[96:97], v[92:93]
	v_pk_mul_f32 v[86:87], v[86:87], v[82:83]
	v_pk_mul_f32 v[88:89], v[88:89], v[84:85]
	v_cvt_pk_fp8_f32 v22, v94, v95
	v_cvt_pk_fp8_f32 v23, v86, v87
	v_cvt_pk_fp8_f32 v22, v96, v97 op_sel:[0,0,1]
	v_cvt_pk_fp8_f32 v23, v88, v89 op_sel:[0,0,1]
	v_add_u32_e32 v31, 0x40000, v21
	s_nop 0
	global_store_dwordx2 v31, v[22:23], s[0:1]
	v_pk_fma_f32 v[78:79], v[78:79], v[18:19], v[14:15] op_sel_hi:[1,0,1]
	v_pk_fma_f32 v[80:81], v[80:81], v[18:19], v[16:17] op_sel_hi:[1,0,1]
	v_pk_fma_f32 v[66:67], v[66:67], v[18:19], v[6:7] op_sel_hi:[1,0,1]
	v_pk_fma_f32 v[68:69], v[68:69], v[18:19], v[8:9] op_sel_hi:[1,0,1]
	v_max_f32_e32 v78, 0xc1898193, v78
	v_max_f32_e32 v79, 0xc1898193, v79
	v_max_f32_e32 v80, 0xc1898193, v80
	v_max_f32_e32 v81, 0xc1898193, v81
	v_max_f32_e32 v66, 0xc1898193, v66
	v_max_f32_e32 v67, 0xc1898193, v67
	v_max_f32_e32 v68, 0xc1898193, v68
	v_max_f32_e32 v69, 0xc1898193, v69
	v_exp_f32_e32 v22, v78
	v_exp_f32_e32 v23, v79
	v_exp_f32_e32 v24, v80
	v_exp_f32_e32 v25, v81
	v_exp_f32_e32 v26, v66
	v_exp_f32_e32 v27, v67
	v_exp_f32_e32 v28, v68
	v_exp_f32_e32 v29, v69
	v_pk_fma_f32 v[74:75], v[74:75], v[20:21], v[10:11] op_sel_hi:[1,0,1]
	v_pk_fma_f32 v[76:77], v[76:77], v[20:21], v[12:13] op_sel_hi:[1,0,1]
	v_pk_fma_f32 v[58:59], v[58:59], v[20:21], v[2:3] op_sel_hi:[1,0,1]
	v_pk_fma_f32 v[60:61], v[60:61], v[20:21], v[4:5] op_sel_hi:[1,0,1]
	v_pk_add_f32 v[22:23], v[22:23], 1.0 op_sel_hi:[1,0]
	v_pk_add_f32 v[24:25], v[24:25], 1.0 op_sel_hi:[1,0]
	v_pk_add_f32 v[26:27], v[26:27], 1.0 op_sel_hi:[1,0]
	v_pk_add_f32 v[28:29], v[28:29], 1.0 op_sel_hi:[1,0]
	v_rcp_f32_e32 v22, v22
	v_rcp_f32_e32 v23, v23
	v_rcp_f32_e32 v24, v24
	v_rcp_f32_e32 v25, v25
	v_rcp_f32_e32 v26, v26
	v_rcp_f32_e32 v27, v27
	v_rcp_f32_e32 v28, v28
	v_rcp_f32_e32 v29, v29
	v_med3_f32 v74, v74, v33, v19
	v_med3_f32 v75, v75, v33, v19
	v_med3_f32 v76, v76, v33, v19
	v_med3_f32 v77, v77, v33, v19
	v_med3_f32 v58, v58, v33, v19
	v_med3_f32 v59, v59, v33, v19
	v_med3_f32 v60, v60, v33, v19
	v_med3_f32 v61, v61, v33, v19
	v_pk_mul_f32 v[78:79], v[78:79], v[22:23]
	v_pk_mul_f32 v[80:81], v[80:81], v[24:25]
	v_pk_mul_f32 v[66:67], v[66:67], v[26:27]
	v_pk_mul_f32 v[68:69], v[68:69], v[28:29]
	v_pk_mul_f32 v[78:79], v[78:79], v[74:75]
	v_pk_mul_f32 v[80:81], v[80:81], v[76:77]
	v_pk_mul_f32 v[66:67], v[66:67], v[58:59]
	v_pk_mul_f32 v[68:69], v[68:69], v[60:61]
	v_cvt_pk_fp8_f32 v26, v78, v79
	v_cvt_pk_fp8_f32 v27, v66, v67
	v_cvt_pk_fp8_f32 v26, v80, v81 op_sel:[0,0,1]
	v_cvt_pk_fp8_f32 v27, v68, v69 op_sel:[0,0,1]
	v_add_u32_e32 v31, 0x48000, v21
	s_nop 0
	global_store_dwordx2 v31, v[26:27], s[0:1]
	v_pk_fma_f32 v[54:55], v[54:55], v[18:19], v[14:15] op_sel_hi:[1,0,1]
	v_pk_fma_f32 v[56:57], v[56:57], v[18:19], v[16:17] op_sel_hi:[1,0,1]
	v_pk_fma_f32 v[46:47], v[46:47], v[18:19], v[6:7] op_sel_hi:[1,0,1]
	v_pk_fma_f32 v[48:49], v[48:49], v[18:19], v[8:9] op_sel_hi:[1,0,1]
	v_max_f32_e32 v54, 0xc1898193, v54
	v_max_f32_e32 v55, 0xc1898193, v55
	v_max_f32_e32 v56, 0xc1898193, v56
	v_max_f32_e32 v57, 0xc1898193, v57
	v_max_f32_e32 v46, 0xc1898193, v46
	v_max_f32_e32 v47, 0xc1898193, v47
	v_max_f32_e32 v48, 0xc1898193, v48
	v_max_f32_e32 v49, 0xc1898193, v49
	v_exp_f32_e32 v22, v54
	v_exp_f32_e32 v23, v55
	v_exp_f32_e32 v24, v56
	v_exp_f32_e32 v25, v57
	v_exp_f32_e32 v26, v46
	v_exp_f32_e32 v27, v47
	v_exp_f32_e32 v28, v48
	v_exp_f32_e32 v29, v49
	v_pk_fma_f32 v[70:71], v[70:71], v[20:21], v[10:11] op_sel_hi:[1,0,1]
	v_pk_fma_f32 v[72:73], v[72:73], v[20:21], v[12:13] op_sel_hi:[1,0,1]
	v_pk_fma_f32 v[62:63], v[62:63], v[20:21], v[2:3] op_sel_hi:[1,0,1]
	v_pk_fma_f32 v[64:65], v[64:65], v[20:21], v[4:5] op_sel_hi:[1,0,1]
	v_pk_add_f32 v[22:23], v[22:23], 1.0 op_sel_hi:[1,0]
	v_pk_add_f32 v[24:25], v[24:25], 1.0 op_sel_hi:[1,0]
	v_pk_add_f32 v[26:27], v[26:27], 1.0 op_sel_hi:[1,0]
	v_pk_add_f32 v[28:29], v[28:29], 1.0 op_sel_hi:[1,0]
	v_rcp_f32_e32 v22, v22
	v_rcp_f32_e32 v23, v23
	v_rcp_f32_e32 v24, v24
	v_rcp_f32_e32 v25, v25
	v_rcp_f32_e32 v26, v26
	v_rcp_f32_e32 v27, v27
	v_rcp_f32_e32 v28, v28
	v_rcp_f32_e32 v29, v29
	v_med3_f32 v70, v70, v33, v19
	v_med3_f32 v71, v71, v33, v19
	v_med3_f32 v72, v72, v33, v19
	v_med3_f32 v73, v73, v33, v19
	v_med3_f32 v62, v62, v33, v19
	v_med3_f32 v63, v63, v33, v19
	v_med3_f32 v64, v64, v33, v19
	v_med3_f32 v65, v65, v33, v19
	v_pk_mul_f32 v[54:55], v[54:55], v[22:23]
	v_pk_mul_f32 v[56:57], v[56:57], v[24:25]
	v_pk_mul_f32 v[46:47], v[46:47], v[26:27]
	v_pk_mul_f32 v[48:49], v[48:49], v[28:29]
	v_pk_mul_f32 v[54:55], v[54:55], v[70:71]
	v_pk_mul_f32 v[56:57], v[56:57], v[72:73]
	v_pk_mul_f32 v[46:47], v[46:47], v[62:63]
	v_pk_mul_f32 v[48:49], v[48:49], v[64:65]
	v_cvt_pk_fp8_f32 v22, v54, v55
	v_cvt_pk_fp8_f32 v23, v46, v47
	v_cvt_pk_fp8_f32 v22, v56, v57 op_sel:[0,0,1]
	v_cvt_pk_fp8_f32 v23, v48, v49 op_sel:[0,0,1]
	v_add_u32_e32 v31, 0x50000, v21
	s_nop 0
	global_store_dwordx2 v31, v[22:23], s[0:1]
	v_pk_fma_f32 v[38:39], v[38:39], v[18:19], v[14:15] op_sel_hi:[1,0,1]
	v_pk_fma_f32 v[40:41], v[40:41], v[18:19], v[16:17] op_sel_hi:[1,0,1]
	v_pk_fma_f32 v[34:35], v[34:35], v[18:19], v[6:7] op_sel_hi:[1,0,1]
	v_pk_fma_f32 v[36:37], v[36:37], v[18:19], v[8:9] op_sel_hi:[1,0,1]
	v_max_f32_e32 v38, 0xc1898193, v38
	v_max_f32_e32 v39, 0xc1898193, v39
	v_max_f32_e32 v40, 0xc1898193, v40
	v_max_f32_e32 v41, 0xc1898193, v41
	v_max_f32_e32 v34, 0xc1898193, v34
	v_max_f32_e32 v35, 0xc1898193, v35
	v_max_f32_e32 v36, 0xc1898193, v36
	v_max_f32_e32 v37, 0xc1898193, v37
	v_exp_f32_e32 v22, v38
	v_exp_f32_e32 v23, v39
	v_exp_f32_e32 v24, v40
	v_exp_f32_e32 v25, v41
	v_exp_f32_e32 v26, v34
	v_exp_f32_e32 v27, v35
	v_exp_f32_e32 v28, v36
	v_exp_f32_e32 v29, v37
	v_pk_fma_f32 v[50:51], v[50:51], v[20:21], v[10:11] op_sel_hi:[1,0,1]
	v_pk_fma_f32 v[52:53], v[52:53], v[20:21], v[12:13] op_sel_hi:[1,0,1]
	v_pk_fma_f32 v[42:43], v[42:43], v[20:21], v[2:3] op_sel_hi:[1,0,1]
	v_pk_fma_f32 v[44:45], v[44:45], v[20:21], v[4:5] op_sel_hi:[1,0,1]
	v_pk_add_f32 v[22:23], v[22:23], 1.0 op_sel_hi:[1,0]
	v_pk_add_f32 v[24:25], v[24:25], 1.0 op_sel_hi:[1,0]
	v_pk_add_f32 v[26:27], v[26:27], 1.0 op_sel_hi:[1,0]
	v_pk_add_f32 v[28:29], v[28:29], 1.0 op_sel_hi:[1,0]
	v_rcp_f32_e32 v22, v22
	v_rcp_f32_e32 v23, v23
	v_rcp_f32_e32 v24, v24
	v_rcp_f32_e32 v25, v25
	v_rcp_f32_e32 v26, v26
	v_rcp_f32_e32 v27, v27
	v_rcp_f32_e32 v28, v28
	v_rcp_f32_e32 v29, v29
	v_med3_f32 v50, v50, v33, v19
	v_med3_f32 v51, v51, v33, v19
	v_med3_f32 v52, v52, v33, v19
	v_med3_f32 v53, v53, v33, v19
	v_med3_f32 v42, v42, v33, v19
	v_med3_f32 v43, v43, v33, v19
	v_med3_f32 v44, v44, v33, v19
	v_med3_f32 v45, v45, v33, v19
	v_pk_mul_f32 v[38:39], v[38:39], v[22:23]
	v_pk_mul_f32 v[40:41], v[40:41], v[24:25]
	v_pk_mul_f32 v[34:35], v[34:35], v[26:27]
	v_pk_mul_f32 v[36:37], v[36:37], v[28:29]
	v_pk_mul_f32 v[38:39], v[38:39], v[50:51]
	v_pk_mul_f32 v[40:41], v[40:41], v[52:53]
	v_pk_mul_f32 v[34:35], v[34:35], v[42:43]
	v_pk_mul_f32 v[36:37], v[36:37], v[44:45]
	v_cvt_pk_fp8_f32 v26, v38, v39
	v_cvt_pk_fp8_f32 v27, v34, v35
	v_cvt_pk_fp8_f32 v26, v40, v41 op_sel:[0,0,1]
	v_cvt_pk_fp8_f32 v27, v36, v37 op_sel:[0,0,1]
	v_add_u32_e32 v31, 0x58000, v21
	s_nop 0
	global_store_dwordx2 v31, v[26:27], s[0:1]
	s_andn2_b64 vcc, exec, s[22:23]
	s_mov_b64 s[22:23], -1
	s_cbranch_vccnz .LBB0_1341
	s_andn2_b64 vcc, exec, s[6:7]
	s_cbranch_vccnz .LBB0_1340
	s_barrier
	s_branch .LBB0_1340
